# P4 weight converter: source loads issued with sc1 (device scope, L1 bypass)
# baseline (speedup 1.0000x reference)
; __device__ __forceinline__ void convert_item(Frame& F, int i0, LAS unsigned char* cvbuf) {
;     { const CvItem c = cv_decode(F, i0);
;         float x[128];
; #pragma unroll
;         for (int i = 0; i < 128; ++i) x[i] = c.src[(size_t)i * c.N];
.LBB0_1092:
	s_lshl_b64 s[16:17], s[16:17], 2
	global_load_dword v16, v[12:13], off sc1
	v_lshl_add_u64 v[12:13], v[12:13], 0, s[16:17]
	v_lshl_add_u64 v[18:19], v[12:13], 0, s[16:17]
	v_lshl_add_u64 v[20:21], v[18:19], 0, s[16:17]
	v_lshl_add_u64 v[22:23], v[20:21], 0, s[16:17]
	v_lshl_add_u64 v[24:25], v[22:23], 0, s[16:17]
	v_lshl_add_u64 v[26:27], v[24:25], 0, s[16:17]
	v_lshl_add_u64 v[28:29], v[26:27], 0, s[16:17]
	v_lshl_add_u64 v[30:31], v[28:29], 0, s[16:17]
	global_load_dword v13, v[12:13], off sc1
	s_nop 0
	global_load_dword v17, v[18:19], off sc1
	s_nop 0
	global_load_dword v18, v[20:21], off sc1
	global_load_dword v19, v[22:23], off sc1
	s_nop 0
	global_load_dword v20, v[24:25], off sc1
	global_load_dword v21, v[26:27], off sc1
	s_nop 0
	global_load_dword v24, v[28:29], off sc1
	global_load_dword v12, v[30:31], off sc1
	v_lshl_add_u64 v[22:23], v[30:31], 0, s[16:17]
	v_lshl_add_u64 v[26:27], v[22:23], 0, s[16:17]
	global_load_dword v22, v[22:23], off sc1
	s_nop 0
	global_load_dword v23, v[26:27], off sc1
	v_lshl_add_u64 v[26:27], v[26:27], 0, s[16:17]
	v_lshl_add_u64 v[28:29], v[26:27], 0, s[16:17]
	v_lshl_add_u64 v[30:31], v[28:29], 0, s[16:17]
	global_load_dword v25, v[26:27], off sc1
	s_andn2_b64 vcc, exec, s[14:15]
	global_load_dword v26, v[28:29], off sc1
	s_mov_b64 s[14:15], -1
	global_load_dword v28, v[30:31], off sc1
	v_lshl_add_u64 v[30:31], v[30:31], 0, s[16:17]
	global_load_dword v29, v[30:31], off sc1
	v_lshl_add_u64 v[30:31], v[30:31], 0, s[16:17]
	global_load_dword v32, v[30:31], off sc1
	v_lshl_add_u64 v[30:31], v[30:31], 0, s[16:17]
	v_lshl_add_u64 v[34:35], v[30:31], 0, s[16:17]
	global_load_dword v27, v[30:31], off sc1
	s_nop 0
	global_load_dword v30, v[34:35], off sc1
	v_lshl_add_u64 v[34:35], v[34:35], 0, s[16:17]
	global_load_dword v31, v[34:35], off sc1
	v_lshl_add_u64 v[34:35], v[34:35], 0, s[16:17]
	v_lshl_add_u64 v[36:37], v[34:35], 0, s[16:17]
	v_lshl_add_u64 v[38:39], v[36:37], 0, s[16:17]
	global_load_dword v33, v[34:35], off sc1
	s_nop 0
	global_load_dword v34, v[36:37], off sc1
	s_nop 0
	global_load_dword v36, v[38:39], off sc1
	v_lshl_add_u64 v[38:39], v[38:39], 0, s[16:17]
	global_load_dword v37, v[38:39], off sc1
	v_lshl_add_u64 v[38:39], v[38:39], 0, s[16:17]
	global_load_dword v40, v[38:39], off sc1
	v_lshl_add_u64 v[38:39], v[38:39], 0, s[16:17]
	v_lshl_add_u64 v[42:43], v[38:39], 0, s[16:17]
	global_load_dword v35, v[38:39], off sc1
	s_nop 0
	global_load_dword v38, v[42:43], off sc1
	v_lshl_add_u64 v[42:43], v[42:43], 0, s[16:17]
	global_load_dword v39, v[42:43], off sc1
	v_lshl_add_u64 v[42:43], v[42:43], 0, s[16:17]
	v_lshl_add_u64 v[44:45], v[42:43], 0, s[16:17]
	v_lshl_add_u64 v[46:47], v[44:45], 0, s[16:17]
	global_load_dword v41, v[42:43], off sc1
	s_nop 0
	global_load_dword v42, v[44:45], off sc1
	s_nop 0
	global_load_dword v44, v[46:47], off sc1
	v_lshl_add_u64 v[46:47], v[46:47], 0, s[16:17]
	global_load_dword v45, v[46:47], off sc1
	v_lshl_add_u64 v[46:47], v[46:47], 0, s[16:17]
	global_load_dword v48, v[46:47], off sc1
	v_lshl_add_u64 v[46:47], v[46:47], 0, s[16:17]
	v_lshl_add_u64 v[50:51], v[46:47], 0, s[16:17]
	global_load_dword v43, v[46:47], off sc1
	s_nop 0
	global_load_dword v46, v[50:51], off sc1
	v_lshl_add_u64 v[50:51], v[50:51], 0, s[16:17]
	global_load_dword v47, v[50:51], off sc1
	v_lshl_add_u64 v[50:51], v[50:51], 0, s[16:17]
	v_lshl_add_u64 v[52:53], v[50:51], 0, s[16:17]
	v_lshl_add_u64 v[54:55], v[52:53], 0, s[16:17]
	global_load_dword v49, v[50:51], off sc1
	s_nop 0
	global_load_dword v50, v[52:53], off sc1
	s_nop 0
	global_load_dword v52, v[54:55], off sc1
	v_lshl_add_u64 v[54:55], v[54:55], 0, s[16:17]
	global_load_dword v53, v[54:55], off sc1
	v_lshl_add_u64 v[54:55], v[54:55], 0, s[16:17]
	global_load_dword v56, v[54:55], off sc1
	v_lshl_add_u64 v[54:55], v[54:55], 0, s[16:17]
	v_lshl_add_u64 v[58:59], v[54:55], 0, s[16:17]
	global_load_dword v51, v[54:55], off sc1
	s_nop 0
	global_load_dword v54, v[58:59], off sc1
	v_lshl_add_u64 v[58:59], v[58:59], 0, s[16:17]
	global_load_dword v55, v[58:59], off sc1
	v_lshl_add_u64 v[58:59], v[58:59], 0, s[16:17]
	v_lshl_add_u64 v[60:61], v[58:59], 0, s[16:17]
	v_lshl_add_u64 v[62:63], v[60:61], 0, s[16:17]
	global_load_dword v57, v[58:59], off sc1
	s_nop 0
	global_load_dword v58, v[60:61], off sc1
	s_nop 0
	global_load_dword v60, v[62:63], off sc1
	v_lshl_add_u64 v[62:63], v[62:63], 0, s[16:17]
	global_load_dword v61, v[62:63], off sc1
	v_lshl_add_u64 v[62:63], v[62:63], 0, s[16:17]
	global_load_dword v64, v[62:63], off sc1
	v_lshl_add_u64 v[62:63], v[62:63], 0, s[16:17]
	v_lshl_add_u64 v[66:67], v[62:63], 0, s[16:17]
	global_load_dword v59, v[62:63], off sc1
	s_nop 0
	global_load_dword v62, v[66:67], off sc1
	v_lshl_add_u64 v[66:67], v[66:67], 0, s[16:17]
	global_load_dword v63, v[66:67], off sc1
	v_lshl_add_u64 v[66:67], v[66:67], 0, s[16:17]
	v_lshl_add_u64 v[68:69], v[66:67], 0, s[16:17]
	v_lshl_add_u64 v[70:71], v[68:69], 0, s[16:17]
	global_load_dword v65, v[66:67], off sc1
	s_nop 0
	global_load_dword v66, v[68:69], off sc1
	s_nop 0
	global_load_dword v68, v[70:71], off sc1
	v_lshl_add_u64 v[70:71], v[70:71], 0, s[16:17]
	global_load_dword v69, v[70:71], off sc1
	v_lshl_add_u64 v[70:71], v[70:71], 0, s[16:17]
	global_load_dword v72, v[70:71], off sc1
	v_lshl_add_u64 v[70:71], v[70:71], 0, s[16:17]
	s_waitcnt vmcnt(62)
; __device__ __forceinline__ void convert_item(Frame& F, int i0, LAS unsigned char* cvbuf) {
;     { const CvItem c = cv_decode(F, i0);
;         float x[128];
; #pragma unroll
;         for (int i = 0; i < 128; ++i) x[i] = c.src[(size_t)i * c.N];
	v_lshl_add_u64 v[74:75], v[70:71], 0, s[16:17]
	global_load_dword v67, v[70:71], off sc1
	s_nop 0
	global_load_dword v70, v[74:75], off sc1
	v_lshl_add_u64 v[74:75], v[74:75], 0, s[16:17]
	global_load_dword v71, v[74:75], off sc1
	v_lshl_add_u64 v[74:75], v[74:75], 0, s[16:17]
	v_lshl_add_u64 v[76:77], v[74:75], 0, s[16:17]
	v_lshl_add_u64 v[78:79], v[76:77], 0, s[16:17]
	global_load_dword v73, v[74:75], off sc1
	s_nop 0
	global_load_dword v74, v[76:77], off sc1
	s_nop 0
	global_load_dword v76, v[78:79], off sc1
	v_lshl_add_u64 v[78:79], v[78:79], 0, s[16:17]
	global_load_dword v77, v[78:79], off sc1
	v_lshl_add_u64 v[78:79], v[78:79], 0, s[16:17]
	global_load_dword v80, v[78:79], off sc1
	v_lshl_add_u64 v[78:79], v[78:79], 0, s[16:17]
	v_lshl_add_u64 v[82:83], v[78:79], 0, s[16:17]
	global_load_dword v75, v[78:79], off sc1
	s_nop 0
	global_load_dword v78, v[82:83], off sc1
	v_lshl_add_u64 v[82:83], v[82:83], 0, s[16:17]
	global_load_dword v79, v[82:83], off sc1
	v_lshl_add_u64 v[82:83], v[82:83], 0, s[16:17]
	v_lshl_add_u64 v[84:85], v[82:83], 0, s[16:17]
	v_lshl_add_u64 v[86:87], v[84:85], 0, s[16:17]
	global_load_dword v81, v[82:83], off sc1
	s_nop 0
	global_load_dword v82, v[84:85], off sc1
	s_nop 0
	global_load_dword v84, v[86:87], off sc1
	v_lshl_add_u64 v[86:87], v[86:87], 0, s[16:17]
	global_load_dword v85, v[86:87], off sc1
	v_lshl_add_u64 v[86:87], v[86:87], 0, s[16:17]
	global_load_dword v88, v[86:87], off sc1
	v_lshl_add_u64 v[86:87], v[86:87], 0, s[16:17]
	v_lshl_add_u64 v[90:91], v[86:87], 0, s[16:17]
	global_load_dword v83, v[86:87], off sc1
	s_nop 0
	global_load_dword v86, v[90:91], off sc1
	v_lshl_add_u64 v[90:91], v[90:91], 0, s[16:17]
	global_load_dword v87, v[90:91], off sc1
	v_lshl_add_u64 v[90:91], v[90:91], 0, s[16:17]
	v_lshl_add_u64 v[92:93], v[90:91], 0, s[16:17]
	v_lshl_add_u64 v[94:95], v[92:93], 0, s[16:17]
	global_load_dword v89, v[90:91], off sc1
	s_nop 0
	global_load_dword v90, v[92:93], off sc1
	s_nop 0
	global_load_dword v92, v[94:95], off sc1
	v_lshl_add_u64 v[94:95], v[94:95], 0, s[16:17]
	global_load_dword v93, v[94:95], off sc1
	v_lshl_add_u64 v[94:95], v[94:95], 0, s[16:17]
	global_load_dword v96, v[94:95], off sc1
	v_lshl_add_u64 v[94:95], v[94:95], 0, s[16:17]
	v_lshl_add_u64 v[98:99], v[94:95], 0, s[16:17]
	global_load_dword v91, v[94:95], off sc1
	s_nop 0
	global_load_dword v94, v[98:99], off sc1
	v_lshl_add_u64 v[98:99], v[98:99], 0, s[16:17]
	global_load_dword v95, v[98:99], off sc1
	v_lshl_add_u64 v[98:99], v[98:99], 0, s[16:17]
	v_lshl_add_u64 v[100:101], v[98:99], 0, s[16:17]
	v_lshl_add_u64 v[102:103], v[100:101], 0, s[16:17]
	global_load_dword v97, v[98:99], off sc1
	s_nop 0
	global_load_dword v98, v[100:101], off sc1
	s_nop 0
	global_load_dword v100, v[102:103], off sc1
	v_lshl_add_u64 v[102:103], v[102:103], 0, s[16:17]
	global_load_dword v101, v[102:103], off sc1
	v_lshl_add_u64 v[102:103], v[102:103], 0, s[16:17]
	global_load_dword v104, v[102:103], off sc1
	v_lshl_add_u64 v[102:103], v[102:103], 0, s[16:17]
	v_lshl_add_u64 v[106:107], v[102:103], 0, s[16:17]
	global_load_dword v99, v[102:103], off sc1
	s_nop 0
	global_load_dword v102, v[106:107], off sc1
	v_lshl_add_u64 v[106:107], v[106:107], 0, s[16:17]
	global_load_dword v103, v[106:107], off sc1
	v_lshl_add_u64 v[106:107], v[106:107], 0, s[16:17]
	v_lshl_add_u64 v[108:109], v[106:107], 0, s[16:17]
	v_lshl_add_u64 v[110:111], v[108:109], 0, s[16:17]
	global_load_dword v105, v[106:107], off sc1
	s_nop 0
	global_load_dword v106, v[108:109], off sc1
	s_nop 0
	global_load_dword v108, v[110:111], off sc1
	v_lshl_add_u64 v[110:111], v[110:111], 0, s[16:17]
	global_load_dword v109, v[110:111], off sc1
	v_lshl_add_u64 v[110:111], v[110:111], 0, s[16:17]
	global_load_dword v112, v[110:111], off sc1
	v_lshl_add_u64 v[110:111], v[110:111], 0, s[16:17]
	v_lshl_add_u64 v[114:115], v[110:111], 0, s[16:17]
	global_load_dword v107, v[110:111], off sc1
	s_nop 0
	global_load_dword v110, v[114:115], off sc1
	v_lshl_add_u64 v[114:115], v[114:115], 0, s[16:17]
	global_load_dword v111, v[114:115], off sc1
	v_lshl_add_u64 v[114:115], v[114:115], 0, s[16:17]
	v_lshl_add_u64 v[116:117], v[114:115], 0, s[16:17]
	v_lshl_add_u64 v[118:119], v[116:117], 0, s[16:17]
	global_load_dword v113, v[114:115], off sc1
	s_nop 0
	global_load_dword v114, v[116:117], off sc1
	s_nop 0
	global_load_dword v116, v[118:119], off sc1
	v_lshl_add_u64 v[118:119], v[118:119], 0, s[16:17]
	global_load_dword v117, v[118:119], off sc1
	v_lshl_add_u64 v[118:119], v[118:119], 0, s[16:17]
	global_load_dword v120, v[118:119], off sc1
	v_lshl_add_u64 v[118:119], v[118:119], 0, s[16:17]
	v_lshl_add_u64 v[122:123], v[118:119], 0, s[16:17]
	global_load_dword v115, v[118:119], off sc1
	s_nop 0
	global_load_dword v118, v[122:123], off sc1
	v_lshl_add_u64 v[122:123], v[122:123], 0, s[16:17]
	global_load_dword v119, v[122:123], off sc1
	v_lshl_add_u64 v[122:123], v[122:123], 0, s[16:17]
	v_lshl_add_u64 v[124:125], v[122:123], 0, s[16:17]
	v_lshl_add_u64 v[126:127], v[124:125], 0, s[16:17]
	global_load_dword v121, v[122:123], off sc1
	s_nop 0
	global_load_dword v122, v[124:125], off sc1
	s_nop 0
	global_load_dword v124, v[126:127], off sc1
	v_lshl_add_u64 v[126:127], v[126:127], 0, s[16:17]
	global_load_dword v125, v[126:127], off sc1
	v_lshl_add_u64 v[126:127], v[126:127], 0, s[16:17]
	global_load_dword v128, v[126:127], off sc1
	v_lshl_add_u64 v[126:127], v[126:127], 0, s[16:17]
	v_lshl_add_u64 v[130:131], v[126:127], 0, s[16:17]
	global_load_dword v123, v[126:127], off sc1
	s_nop 0
	global_load_dword v126, v[130:131], off sc1
	v_lshl_add_u64 v[130:131], v[130:131], 0, s[16:17]
	global_load_dword v127, v[130:131], off sc1
	v_lshl_add_u64 v[130:131], v[130:131], 0, s[16:17]
	v_lshl_add_u64 v[132:133], v[130:131], 0, s[16:17]
	s_waitcnt vmcnt(62)
	v_lshl_add_u64 v[134:135], v[132:133], 0, s[16:17]
	global_load_dword v129, v[130:131], off sc1
	s_nop 0
	global_load_dword v130, v[132:133], off sc1
	s_nop 0
	global_load_dword v132, v[134:135], off sc1
	v_lshl_add_u64 v[134:135], v[134:135], 0, s[16:17]
	global_load_dword v133, v[134:135], off sc1
	v_lshl_add_u64 v[134:135], v[134:135], 0, s[16:17]
	global_load_dword v136, v[134:135], off sc1
	v_lshl_add_u64 v[134:135], v[134:135], 0, s[16:17]
	v_lshl_add_u64 v[138:139], v[134:135], 0, s[16:17]
	global_load_dword v131, v[134:135], off sc1
	s_nop 0
	global_load_dword v134, v[138:139], off sc1
	v_lshl_add_u64 v[138:139], v[138:139], 0, s[16:17]
	global_load_dword v135, v[138:139], off sc1
	v_lshl_add_u64 v[138:139], v[138:139], 0, s[16:17]
	s_waitcnt vmcnt(62)
	v_lshl_add_u64 v[140:141], v[138:139], 0, s[16:17]
	global_load_dword v137, v[138:139], off sc1
	s_nop 0
	global_load_dword v138, v[140:141], off sc1
	v_lshl_add_u64 v[140:141], v[140:141], 0, s[16:17]
	v_lshl_add_u64 v[142:143], v[140:141], 0, s[16:17]
	global_load_dword v139, v[140:141], off sc1
	s_nop 0
	global_load_dword v140, v[142:143], off sc1
	v_lshl_add_u64 v[142:143], v[142:143], 0, s[16:17]
	global_load_dword v141, v[142:143], off sc1
	s_cbranch_vccz .LBB0_1094
; #define LAS __attribute__((address_space(3)))
; __device__ __forceinline__ unsigned pk4f8(float a, float b, float c, float d) { int r = 0; r = __builtin_amdgcn_cvt_pk_fp8_f32(a, b, r, false); r = __builtin_amdgcn_cvt_pk_fp8_f32(c, d, r, true); return (unsigned)r; }
; __device__ __forceinline__ void convert_item(Frame& F, int i0, LAS unsigned char* cvbuf) {
;     ...
;         if (c.f8) {
;             const int lane = F.lane; LAS unsigned char* bw = cvbuf + lane * 144;
; #pragma unroll
;             for (int q = 0; q < 8; ++q) { v4u o; o.x = pk4f8(x[16 * q + 0] * F8_SW, x[16 * q + 1] * F8_SW, x[16 * q + 2] * F8_SW, x[16 * q + 3] * F8_SW); o.y = pk4f8(x[16 * q + 4] * F8_SW, x[16 * q + 5] * F8_SW, x[16 * q + 6] * F8_SW, x[16 * q + 7] * F8_SW);
;                 o.z = pk4f8(x[16 * q + 8] * F8_SW, x[16 * q + 9] * F8_SW, x[16 * q + 10] * F8_SW, x[16 * q + 11] * F8_SW); o.w = pk4f8(x[16 * q + 12] * F8_SW, x[16 * q + 13] * F8_SW, x[16 * q + 14] * F8_SW, x[16 * q + 15] * F8_SW);
;                 *(LAS v4u*)(bw + 16 * q) = o; }
	v_mul_f32_e32 v143, 0x43800000, v16
	v_mul_f32_e32 v144, 0x43800000, v13
	v_mov_b32_e32 v142, v3
	v_cvt_pk_fp8_f32 v142, v143, v144
	v_mul_f32_e32 v144, 0x43800000, v19
	v_mul_f32_e32 v147, 0x43800000, v20
	v_mov_b32_e32 v143, v3
	v_cvt_pk_fp8_f32 v143, v144, v147
	v_mul_f32_e32 v145, 0x43800000, v17
	v_mul_f32_e32 v146, 0x43800000, v18
	v_cvt_pk_fp8_f32 v142, v145, v146 op_sel:[0,0,1]
	v_mul_f32_e32 v144, 0x43800000, v21
	v_mul_f32_e32 v145, 0x43800000, v24
	v_cvt_pk_fp8_f32 v143, v144, v145 op_sel:[0,0,1]
	v_mul_f32_e32 v145, 0x43800000, v12
	v_mul_f32_e32 v146, 0x43800000, v22
	v_mov_b32_e32 v144, v3
	v_cvt_pk_fp8_f32 v144, v145, v146
	v_mul_f32_e32 v146, 0x43800000, v26
	v_mul_f32_e32 v149, 0x43800000, v28
	v_mov_b32_e32 v145, v3
	v_cvt_pk_fp8_f32 v145, v146, v149
	v_mul_f32_e32 v147, 0x43800000, v23
	v_mul_f32_e32 v148, 0x43800000, v25
	v_cvt_pk_fp8_f32 v144, v147, v148 op_sel:[0,0,1]
	v_mul_f32_e32 v146, 0x43800000, v29
	v_mul_f32_e32 v147, 0x43800000, v32
	v_cvt_pk_fp8_f32 v145, v146, v147 op_sel:[0,0,1]
	v_mul_f32_e32 v147, 0x43800000, v27
	v_mul_f32_e32 v148, 0x43800000, v30
	v_mov_b32_e32 v146, v3
	v_cvt_pk_fp8_f32 v146, v147, v148
	v_mul_f32_e32 v148, 0x43800000, v34
	v_mul_f32_e32 v151, 0x43800000, v36
	v_mov_b32_e32 v147, v3
	v_cvt_pk_fp8_f32 v147, v148, v151
	v_mul_f32_e32 v149, 0x43800000, v31
	v_mul_f32_e32 v150, 0x43800000, v33
	v_cvt_pk_fp8_f32 v146, v149, v150 op_sel:[0,0,1]
	v_mul_f32_e32 v148, 0x43800000, v37
	v_mul_f32_e32 v149, 0x43800000, v40
	v_cvt_pk_fp8_f32 v147, v148, v149 op_sel:[0,0,1]
	v_mul_f32_e32 v149, 0x43800000, v35
	v_mul_f32_e32 v150, 0x43800000, v38
	v_mov_b32_e32 v148, v3
	v_cvt_pk_fp8_f32 v148, v149, v150
	v_mul_f32_e32 v150, 0x43800000, v42
	v_mul_f32_e32 v153, 0x43800000, v44
	v_mov_b32_e32 v149, v3
	v_cvt_pk_fp8_f32 v149, v150, v153
	v_mul_f32_e32 v151, 0x43800000, v39
	v_mul_f32_e32 v152, 0x43800000, v41
	v_cvt_pk_fp8_f32 v148, v151, v152 op_sel:[0,0,1]
	v_mul_f32_e32 v150, 0x43800000, v45
	v_mul_f32_e32 v151, 0x43800000, v48
	v_cvt_pk_fp8_f32 v149, v150, v151 op_sel:[0,0,1]
	v_mul_f32_e32 v151, 0x43800000, v43
	v_mul_f32_e32 v152, 0x43800000, v46
	v_mov_b32_e32 v150, v3
	v_cvt_pk_fp8_f32 v150, v151, v152
	v_mul_f32_e32 v152, 0x43800000, v50
	v_mul_f32_e32 v155, 0x43800000, v52
	v_mov_b32_e32 v151, v3
	v_cvt_pk_fp8_f32 v151, v152, v155
	v_mul_f32_e32 v153, 0x43800000, v47
	v_mul_f32_e32 v154, 0x43800000, v49
	v_cvt_pk_fp8_f32 v150, v153, v154 op_sel:[0,0,1]
	v_mul_f32_e32 v152, 0x43800000, v53
	v_mul_f32_e32 v153, 0x43800000, v56
	v_cvt_pk_fp8_f32 v151, v152, v153 op_sel:[0,0,1]
	v_mul_f32_e32 v153, 0x43800000, v51
	v_mul_f32_e32 v154, 0x43800000, v54
	v_mov_b32_e32 v152, v3
	v_cvt_pk_fp8_f32 v152, v153, v154
	v_mul_f32_e32 v154, 0x43800000, v58
	v_mul_f32_e32 v157, 0x43800000, v60
	v_mov_b32_e32 v153, v3
	v_cvt_pk_fp8_f32 v153, v154, v157
	v_mul_f32_e32 v155, 0x43800000, v55
	v_mul_f32_e32 v156, 0x43800000, v57
	v_cvt_pk_fp8_f32 v152, v155, v156 op_sel:[0,0,1]
	v_mul_f32_e32 v154, 0x43800000, v61
	v_mul_f32_e32 v155, 0x43800000, v64
	v_cvt_pk_fp8_f32 v153, v154, v155 op_sel:[0,0,1]
	v_mul_f32_e32 v155, 0x43800000, v59
	v_mul_f32_e32 v156, 0x43800000, v62
	v_mov_b32_e32 v154, v3
	v_cvt_pk_fp8_f32 v154, v155, v156
	v_mul_f32_e32 v156, 0x43800000, v66
	v_mul_f32_e32 v159, 0x43800000, v68
	v_mov_b32_e32 v155, v3
	v_cvt_pk_fp8_f32 v155, v156, v159
	v_mul_f32_e32 v157, 0x43800000, v63
	v_mul_f32_e32 v158, 0x43800000, v65
	v_cvt_pk_fp8_f32 v154, v157, v158 op_sel:[0,0,1]
	v_mul_f32_e32 v156, 0x43800000, v69
	v_mul_f32_e32 v157, 0x43800000, v72
	v_cvt_pk_fp8_f32 v155, v156, v157 op_sel:[0,0,1]
	v_mul_f32_e32 v157, 0x43800000, v67
	v_mul_f32_e32 v158, 0x43800000, v70
	v_mov_b32_e32 v156, v3
	v_cvt_pk_fp8_f32 v156, v157, v158
	v_mul_f32_e32 v158, 0x43800000, v74
	s_waitcnt vmcnt(62)
	v_mul_f32_e32 v161, 0x43800000, v76
	v_mov_b32_e32 v157, v3
	v_cvt_pk_fp8_f32 v157, v158, v161
	v_mul_f32_e32 v159, 0x43800000, v71
	v_mul_f32_e32 v160, 0x43800000, v73
	v_cvt_pk_fp8_f32 v156, v159, v160 op_sel:[0,0,1]
	v_mul_f32_e32 v158, 0x43800000, v77
	v_mul_f32_e32 v159, 0x43800000, v80
	v_cvt_pk_fp8_f32 v157, v158, v159 op_sel:[0,0,1]
	ds_write_b128 v14, v[142:145] offset:8192
	ds_write_b128 v14, v[146:149] offset:8208
	ds_write_b128 v14, v[150:153] offset:8224
	ds_write_b128 v14, v[154:157] offset:8240
	v_mul_f32_e32 v143, 0x43800000, v75
	v_mul_f32_e32 v144, 0x43800000, v78
	v_mov_b32_e32 v142, v3
	v_cvt_pk_fp8_f32 v142, v143, v144
	s_waitcnt vmcnt(59)
	v_mul_f32_e32 v144, 0x43800000, v82
	s_waitcnt vmcnt(58)
	v_mul_f32_e32 v147, 0x43800000, v84
	v_mov_b32_e32 v143, v3
	v_cvt_pk_fp8_f32 v143, v144, v147
	v_mul_f32_e32 v145, 0x43800000, v79
	v_mul_f32_e32 v146, 0x43800000, v81
	v_cvt_pk_fp8_f32 v142, v145, v146 op_sel:[0,0,1]
	s_waitcnt vmcnt(57)
	v_mul_f32_e32 v144, 0x43800000, v85
	s_waitcnt vmcnt(56)
	v_mul_f32_e32 v145, 0x43800000, v88
	v_cvt_pk_fp8_f32 v143, v144, v145 op_sel:[0,0,1]
	s_waitcnt vmcnt(55)
	v_mul_f32_e32 v145, 0x43800000, v83
	s_waitcnt vmcnt(54)
	v_mul_f32_e32 v146, 0x43800000, v86
	v_mov_b32_e32 v144, v3
	v_cvt_pk_fp8_f32 v144, v145, v146
	s_waitcnt vmcnt(51)
	v_mul_f32_e32 v146, 0x43800000, v90
	s_waitcnt vmcnt(50)
	v_mul_f32_e32 v149, 0x43800000, v92
	v_mov_b32_e32 v145, v3
	v_cvt_pk_fp8_f32 v145, v146, v149
	v_mul_f32_e32 v147, 0x43800000, v87
	v_mul_f32_e32 v148, 0x43800000, v89
	v_cvt_pk_fp8_f32 v144, v147, v148 op_sel:[0,0,1]
	s_waitcnt vmcnt(49)
	v_mul_f32_e32 v146, 0x43800000, v93
	s_waitcnt vmcnt(48)
	v_mul_f32_e32 v147, 0x43800000, v96
	v_cvt_pk_fp8_f32 v145, v146, v147 op_sel:[0,0,1]
	s_waitcnt vmcnt(47)
	v_mul_f32_e32 v147, 0x43800000, v91
	s_waitcnt vmcnt(46)
; #define LAS __attribute__((address_space(3)))
; __device__ __forceinline__ unsigned pk4f8(float a, float b, float c, float d) { int r = 0; r = __builtin_amdgcn_cvt_pk_fp8_f32(a, b, r, false); r = __builtin_amdgcn_cvt_pk_fp8_f32(c, d, r, true); return (unsigned)r; }
; __device__ __forceinline__ void convert_item(Frame& F, int i0, LAS unsigned char* cvbuf) {
;     ...
;             for (int q = 0; q < 8; ++q) { v4u o; o.x = pk4f8(x[16 * q + 0] * F8_SW, x[16 * q + 1] * F8_SW, x[16 * q + 2] * F8_SW, x[16 * q + 3] * F8_SW); o.y = pk4f8(x[16 * q + 4] * F8_SW, x[16 * q + 5] * F8_SW, x[16 * q + 6] * F8_SW, x[16 * q + 7] * F8_SW);
;                 o.z = pk4f8(x[16 * q + 8] * F8_SW, x[16 * q + 9] * F8_SW, x[16 * q + 10] * F8_SW, x[16 * q + 11] * F8_SW); o.w = pk4f8(x[16 * q + 12] * F8_SW, x[16 * q + 13] * F8_SW, x[16 * q + 14] * F8_SW, x[16 * q + 15] * F8_SW);
;                 *(LAS v4u*)(bw + 16 * q) = o; }
;             unsigned char* d0 = c.dst - (size_t)lane * 2048 + (size_t)(lane >> 3) * 2048 + (lane & 7) * 16; const LAS unsigned char* br = cvbuf + (lane >> 3) * 144 + (lane & 7) * 16;
; #pragma unroll
;             for (int i = 0; i < 8; ++i) { const v4u v = *(const LAS v4u*)(br + i * 8 * 144); *(v4u*)(d0 + (size_t)i * 8 * 2048) = v; } }
	v_mul_f32_e32 v148, 0x43800000, v94
	v_mov_b32_e32 v146, v3
	v_cvt_pk_fp8_f32 v146, v147, v148
	s_waitcnt vmcnt(43)
	v_mul_f32_e32 v148, 0x43800000, v98
	s_waitcnt vmcnt(42)
	v_mul_f32_e32 v151, 0x43800000, v100
	v_mov_b32_e32 v147, v3
	v_cvt_pk_fp8_f32 v147, v148, v151
	v_mul_f32_e32 v149, 0x43800000, v95
	v_mul_f32_e32 v150, 0x43800000, v97
	v_cvt_pk_fp8_f32 v146, v149, v150 op_sel:[0,0,1]
	s_waitcnt vmcnt(41)
	v_mul_f32_e32 v148, 0x43800000, v101
	s_waitcnt vmcnt(40)
	v_mul_f32_e32 v149, 0x43800000, v104
	v_cvt_pk_fp8_f32 v147, v148, v149 op_sel:[0,0,1]
	s_waitcnt vmcnt(39)
	v_mul_f32_e32 v149, 0x43800000, v99
	s_waitcnt vmcnt(38)
	v_mul_f32_e32 v150, 0x43800000, v102
	v_mov_b32_e32 v148, v3
	v_cvt_pk_fp8_f32 v148, v149, v150
	s_waitcnt vmcnt(35)
	v_mul_f32_e32 v150, 0x43800000, v106
	s_waitcnt vmcnt(34)
	v_mul_f32_e32 v153, 0x43800000, v108
	v_mov_b32_e32 v149, v3
	v_cvt_pk_fp8_f32 v149, v150, v153
	v_mul_f32_e32 v151, 0x43800000, v103
	v_mul_f32_e32 v152, 0x43800000, v105
	v_cvt_pk_fp8_f32 v148, v151, v152 op_sel:[0,0,1]
	s_waitcnt vmcnt(33)
	v_mul_f32_e32 v150, 0x43800000, v109
	s_waitcnt vmcnt(32)
	v_mul_f32_e32 v151, 0x43800000, v112
	v_cvt_pk_fp8_f32 v149, v150, v151 op_sel:[0,0,1]
	s_waitcnt vmcnt(31)
	v_mul_f32_e32 v151, 0x43800000, v107
	s_waitcnt vmcnt(30)
	v_mul_f32_e32 v152, 0x43800000, v110
	v_mov_b32_e32 v150, v3
	v_cvt_pk_fp8_f32 v150, v151, v152
	s_waitcnt vmcnt(27)
	v_mul_f32_e32 v152, 0x43800000, v114
	s_waitcnt vmcnt(26)
	v_mul_f32_e32 v155, 0x43800000, v116
	v_mov_b32_e32 v151, v3
	v_cvt_pk_fp8_f32 v151, v152, v155
	v_mul_f32_e32 v153, 0x43800000, v111
	v_mul_f32_e32 v154, 0x43800000, v113
	v_cvt_pk_fp8_f32 v150, v153, v154 op_sel:[0,0,1]
	s_waitcnt vmcnt(25)
	v_mul_f32_e32 v152, 0x43800000, v117
	s_waitcnt vmcnt(24)
	v_mul_f32_e32 v153, 0x43800000, v120
	v_cvt_pk_fp8_f32 v151, v152, v153 op_sel:[0,0,1]
	s_waitcnt vmcnt(23)
	v_mul_f32_e32 v153, 0x43800000, v115
	s_waitcnt vmcnt(22)
	v_mul_f32_e32 v154, 0x43800000, v118
	v_mov_b32_e32 v152, v3
	v_cvt_pk_fp8_f32 v152, v153, v154
	s_waitcnt vmcnt(19)
	v_mul_f32_e32 v154, 0x43800000, v122
	s_waitcnt vmcnt(18)
	v_mul_f32_e32 v157, 0x43800000, v124
	v_mov_b32_e32 v153, v3
	v_cvt_pk_fp8_f32 v153, v154, v157
	v_mul_f32_e32 v155, 0x43800000, v119
	v_mul_f32_e32 v156, 0x43800000, v121
	v_cvt_pk_fp8_f32 v152, v155, v156 op_sel:[0,0,1]
	s_waitcnt vmcnt(17)
	v_mul_f32_e32 v154, 0x43800000, v125
	s_waitcnt vmcnt(16)
	v_mul_f32_e32 v155, 0x43800000, v128
	v_cvt_pk_fp8_f32 v153, v154, v155 op_sel:[0,0,1]
	s_waitcnt vmcnt(15)
	v_mul_f32_e32 v155, 0x43800000, v123
	s_waitcnt vmcnt(14)
	v_mul_f32_e32 v156, 0x43800000, v126
	v_mov_b32_e32 v154, v3
	v_cvt_pk_fp8_f32 v154, v155, v156
	s_waitcnt vmcnt(11)
	v_mul_f32_e32 v156, 0x43800000, v130
	s_waitcnt vmcnt(10)
	v_mul_f32_e32 v159, 0x43800000, v132
	v_mov_b32_e32 v155, v3
	v_cvt_pk_fp8_f32 v155, v156, v159
	v_mul_f32_e32 v157, 0x43800000, v127
	v_mul_f32_e32 v158, 0x43800000, v129
	v_cvt_pk_fp8_f32 v154, v157, v158 op_sel:[0,0,1]
	s_waitcnt vmcnt(9)
	v_mul_f32_e32 v156, 0x43800000, v133
	s_waitcnt vmcnt(8)
	v_mul_f32_e32 v157, 0x43800000, v136
	v_cvt_pk_fp8_f32 v155, v156, v157 op_sel:[0,0,1]
	s_waitcnt vmcnt(7)
	v_mul_f32_e32 v157, 0x43800000, v131
	s_waitcnt vmcnt(6)
	v_mul_f32_e32 v158, 0x43800000, v134
	v_mov_b32_e32 v156, v3
	v_cvt_pk_fp8_f32 v156, v157, v158
	s_waitcnt vmcnt(3)
	v_mul_f32_e32 v158, 0x43800000, v138
	s_waitcnt vmcnt(2)
	v_mul_f32_e32 v161, 0x43800000, v139
	v_mov_b32_e32 v157, v3
	v_cvt_pk_fp8_f32 v157, v158, v161
	v_mul_f32_e32 v159, 0x43800000, v135
	v_mul_f32_e32 v160, 0x43800000, v137
	v_cvt_pk_fp8_f32 v156, v159, v160 op_sel:[0,0,1]
	s_waitcnt vmcnt(1)
	v_mul_f32_e32 v158, 0x43800000, v140
	s_waitcnt vmcnt(0)
	v_mul_f32_e32 v159, 0x43800000, v141
	v_cvt_pk_fp8_f32 v157, v158, v159 op_sel:[0,0,1]
	ds_write_b128 v14, v[142:145] offset:8256
	ds_write_b128 v14, v[146:149] offset:8272
	ds_write_b128 v14, v[150:153] offset:8288
	ds_write_b128 v14, v[154:157] offset:8304
	ds_read_b128 v[142:145], v15 offset:8192
	v_lshl_add_u64 v[146:147], v[10:11], 0, v[4:5]
	v_lshl_add_u64 v[146:147], v[146:147], 0, v[6:7]
	v_lshl_add_u64 v[150:151], v[146:147], 0, v[8:9]
	ds_read_b128 v[146:149], v15 offset:9344
	s_waitcnt lgkmcnt(1)
	global_store_dwordx4 v[150:151], v[142:145], off
	s_mov_b64 s[14:15], 0
	s_nop 0
	v_add_co_u32_e32 v142, vcc, s24, v150
	s_nop 1
	v_addc_co_u32_e32 v143, vcc, 0, v151, vcc
	s_waitcnt lgkmcnt(0)
	global_store_dwordx4 v[142:143], v[146:149], off
	ds_read_b128 v[142:145], v15 offset:10496
	ds_read_b128 v[146:149], v15 offset:11648
	v_add_co_u32_e32 v152, vcc, s25, v150
	s_nop 1
	v_addc_co_u32_e32 v153, vcc, 0, v151, vcc
	s_waitcnt lgkmcnt(1)
	global_store_dwordx4 v[152:153], v[142:145], off
	s_nop 1
	v_add_co_u32_e32 v142, vcc, s26, v150
	s_nop 1
	v_addc_co_u32_e32 v143, vcc, 0, v151, vcc
	s_waitcnt lgkmcnt(0)
	global_store_dwordx4 v[142:143], v[146:149], off
	ds_read_b128 v[142:145], v15 offset:12800
	ds_read_b128 v[146:149], v15 offset:13952
	v_add_co_u32_e32 v152, vcc, s27, v150
	s_nop 1
	v_addc_co_u32_e32 v153, vcc, 0, v151, vcc
	s_waitcnt lgkmcnt(1)
	global_store_dwordx4 v[152:153], v[142:145], off
	s_nop 1
	v_add_co_u32_e32 v142, vcc, 0x14000, v150
	s_nop 1
	v_addc_co_u32_e32 v143, vcc, 0, v151, vcc
	s_waitcnt lgkmcnt(0)
	global_store_dwordx4 v[142:143], v[146:149], off
	ds_read_b128 v[142:145], v15 offset:15104
	ds_read_b128 v[146:149], v15 offset:16256
	v_add_co_u32_e32 v152, vcc, 0x18000, v150
	s_nop 1
	v_addc_co_u32_e32 v153, vcc, 0, v151, vcc
	s_waitcnt lgkmcnt(1)
	global_store_dwordx4 v[152:153], v[142:145], off
	s_nop 1
	v_add_co_u32_e32 v142, vcc, 0x1c000, v150
	s_nop 1
	v_addc_co_u32_e32 v143, vcc, 0, v151, vcc
	s_waitcnt lgkmcnt(0)
	global_store_dwordx4 v[142:143], v[146:149], off
